# P2a: cnorm_rows4 + kic_rows8 folded into wave 4's idle slot of dn_intra stage X (loads issued before S0, processed after); post-loop cnorm/kic passes removed
# speedup vs baseline: 1.0330x; 1.0054x over previous
.LBB0_372:
	s_or_b64 exec, exec, s[0:1]
	s_waitcnt lgkmcnt(0)
	s_barrier
	s_cmp_gt_u32 s77, 63
	s_mov_b64 s[0:1], -1
	s_cbranch_scc0 .LBB0_397
	s_cmp_lg_u32 s78, 4
	s_cbranch_scc1 .Lcn_a_skip
	s_lshr_b32 s81, s96, 3
	s_lshl_b32 s81, s81, 6
	s_lshl_b32 s85, s75, 4
	s_add_i32 s81, s81, s85
	s_lshl_b32 s85, s81, 13
	s_add_u32 s82, s38, s85
	s_addc_u32 s83, s39, 0
	s_add_u32 s82, s82, 0x1e00
	s_addc_u32 s83, s83, 0
	v_lshrrev_b32_e32 v238, 4, v100
	v_and_b32_e32 v239, 15, v100
	v_lshlrev_b32_e32 v240, 4, v239
	v_lshl_or_b32 v232, v238, 13, v240
	v_lshl_or_b32 v235, v238, 8, v240
	v_lshlrev_b32_e32 v234, 5, v239
	v_lshrrev_b32_e32 v238, 3, v100
	v_and_b32_e32 v239, 7, v100
	v_lshlrev_b32_e32 v240, 4, v239
	v_lshl_or_b32 v233, v238, 13, v240
	v_lshl_or_b32 v236, v238, 7, v240
	global_load_dwordx4 v[200:203], v232, s[82:83]
	global_load_dwordx4 v[216:219], v233, s[82:83] offset:256
	s_add_u32 s82, s82, 0x8000
	s_addc_u32 s83, s83, 0
	global_load_dwordx4 v[204:207], v232, s[82:83]
	s_add_u32 s82, s82, 0x8000
	s_addc_u32 s83, s83, 0
	global_load_dwordx4 v[208:211], v232, s[82:83]
	global_load_dwordx4 v[220:223], v233, s[82:83] offset:256
	s_add_u32 s82, s82, 0x8000
	s_addc_u32 s83, s83, 0
	global_load_dwordx4 v[212:215], v232, s[82:83]
	global_load_dwordx4 v[224:227], v234, s[66:67]
	global_load_dwordx4 v[228:231], v234, s[66:67] offset:16
.Lcn_a_skip:
	s_andn2_b64 vcc, exec, s[16:17]
	s_cbranch_vccnz .LBB0_396
	s_cmp_lg_u32 s78, 4
	s_cbranch_scc0 .LBB0_392
	s_waitcnt vmcnt(0)
	v_lshlrev_b32_e32 v102, 16, v86
	v_and_b32_e32 v103, 0xffff0000, v86
	v_lshlrev_b32_e32 v96, 16, v87
	v_and_b32_e32 v97, 0xffff0000, v87
	v_lshlrev_b32_e32 v86, 16, v82
	v_and_b32_e32 v87, 0xffff0000, v82
	v_lshlrev_b32_e32 v14, 16, v83
	v_and_b32_e32 v15, 0xffff0000, v83
	v_lshlrev_b32_e32 v16, 16, v74
	v_and_b32_e32 v17, 0xffff0000, v74
	v_pk_mul_f32 v[82:83], v[38:39], v[102:103]
	v_lshlrev_b32_e32 v8, 16, v90
	v_pk_fma_f32 v[16:17], v[34:35], v[16:17], v[82:83]
	v_and_b32_e32 v9, 0xffff0000, v90
	v_pk_fma_f32 v[16:17], v[46:47], v[86:87], v[16:17]
	v_lshlrev_b32_e32 v12, 16, v84
	v_pk_fma_f32 v[16:17], v[50:51], v[8:9], v[16:17]
	v_and_b32_e32 v13, 0xffff0000, v84
	v_mul_f32_e32 v82, 0xbfb8aa3b, v17
	v_exp_f32_e32 v82, v82
	v_lshlrev_b32_e32 v10, 16, v85
	v_and_b32_e32 v11, 0xffff0000, v85
	v_and_b32_e32 v83, 0xffff0000, v75
	v_add_f32_e32 v90, 1.0, v82
	v_lshlrev_b32_e32 v82, 16, v75
	v_pk_mul_f32 v[84:85], v[40:41], v[96:97]
	v_lshlrev_b32_e32 v6, 16, v91
	v_pk_fma_f32 v[82:83], v[36:37], v[82:83], v[84:85]
	v_and_b32_e32 v7, 0xffff0000, v91
	v_pk_fma_f32 v[82:83], v[48:49], v[14:15], v[82:83]
	v_lshlrev_b32_e32 v94, 16, v88
	v_pk_fma_f32 v[82:83], v[52:53], v[6:7], v[82:83]
	v_and_b32_e32 v95, 0xffff0000, v88
	v_mul_f32_e32 v75, 0xbfb8aa3b, v82
	v_exp_f32_e32 v84, v75
	v_mul_f32_e32 v75, 0xbfb8aa3b, v83
	v_exp_f32_e32 v85, v75
	v_lshlrev_b32_e32 v4, 16, v92
	v_add_f32_e32 v84, 1.0, v84
	v_and_b32_e32 v5, 0xffff0000, v92
	v_lshlrev_b32_e32 v2, 16, v93
	v_and_b32_e32 v3, 0xffff0000, v93
	v_rcp_f32_e32 v75, v90
	v_rcp_f32_e32 v90, v84
	v_add_f32_e32 v91, 1.0, v85
	v_lshlrev_b32_e32 v84, 16, v76
	v_and_b32_e32 v85, 0xffff0000, v76
	v_pk_mul_f32 v[92:93], v[22:23], v[94:95]
	v_lshlrev_b32_e32 v88, 16, v89
	v_pk_fma_f32 v[84:85], v[18:19], v[84:85], v[92:93]
	v_and_b32_e32 v89, 0xffff0000, v89
	v_pk_fma_f32 v[84:85], v[26:27], v[12:13], v[84:85]
	v_pk_mul_f32 v[104:105], v[24:25], v[88:89]
	v_pk_fma_f32 v[92:93], v[30:31], v[4:5], v[84:85]
	v_and_b32_e32 v85, 0xffff0000, v77
	v_mul_f32_e32 v84, 0xbfb8aa3b, v93
	v_exp_f32_e32 v84, v84
	v_mul_f32_e32 v74, 0xbfb8aa3b, v16
	v_mul_f32_e32 v76, 0xbfb8aa3b, v92
	v_exp_f32_e32 v74, v74
	v_add_f32_e32 v115, 1.0, v84
	v_lshlrev_b32_e32 v84, 16, v77
	v_pk_fma_f32 v[84:85], v[20:21], v[84:85], v[104:105]
	v_exp_f32_e32 v76, v76
	v_pk_fma_f32 v[84:85], v[28:29], v[10:11], v[84:85]
	s_ashr_i32 s22, s80, 1
	v_pk_fma_f32 v[104:105], v[32:33], v[2:3], v[84:85]
	s_cmp_lg_u32 s22, 2
	v_mul_f32_e32 v77, 0xbfb8aa3b, v104
	v_exp_f32_e32 v84, v77
	v_mul_f32_e32 v77, 0xbfb8aa3b, v105
	v_exp_f32_e32 v85, v77
	s_cselect_b64 s[0:1], -1, 0
	v_add_f32_e32 v84, 1.0, v84
	s_cmpk_lt_u32 s10, 0x80
	v_add_f32_e32 v74, 1.0, v74
	v_add_f32_e32 v76, 1.0, v76
	v_rcp_f32_e32 v116, v84
	v_add_f32_e32 v84, 1.0, v85
	s_cselect_b64 s[4:5], -1, 0
	v_rcp_f32_e32 v74, v74
	v_rcp_f32_e32 v91, v91
	v_rcp_f32_e32 v76, v76
	v_rcp_f32_e32 v77, v115
	v_rcp_f32_e32 v117, v84
	s_and_b64 s[24:25], s[4:5], exec
	s_cselect_b32 s10, 0x400, s56
	v_lshlrev_b32_e32 v114, 3, v113
	s_add_i32 s10, s33, s10
	v_and_b32_e32 v98, 56, v114
	s_cmp_eq_u32 s22, 2
	v_pk_mul_f32 v[84:85], v[16:17], v[74:75]
	v_pk_mul_f32 v[90:91], v[82:83], v[90:91]
	v_pk_mul_f32 v[92:93], v[92:93], v[76:77]
	v_pk_mul_f32 v[104:105], v[104:105], v[116:117]
	s_cbranch_scc1 .LBB0_377
	v_pk_mul_f32 v[16:17], v[84:85], v[84:85]
	v_pk_mul_f32 v[74:75], v[90:91], v[90:91]
	v_add_f32_e32 v16, v16, v17
	v_add_f32_e32 v16, v74, v16
	v_pk_mul_f32 v[76:77], v[92:93], v[92:93]
	v_add_f32_e32 v16, v75, v16
	v_add_f32_e32 v16, v16, v76
	v_pk_mul_f32 v[82:83], v[104:105], v[104:105]
	v_add_f32_e32 v16, v77, v16
	v_add_f32_e32 v16, v82, v16
	v_add_f32_e32 v16, v83, v16
	v_lshl_add_u32 v17, v98, 2, s10
	ds_add_f32 v17, v16

.LBB0_396:
	s_cmp_lg_u32 s78, 4
	s_cbranch_scc1 .Lcn_b_skip
	s_lshr_b32 s81, s96, 3
	s_lshl_b32 s81, s81, 6
	s_lshl_b32 s85, s75, 4
	s_add_i32 s81, s81, s85
	s_lshl_b32 s85, s81, 8
	s_add_u32 s82, s50, s85
	s_addc_u32 s83, s51, 0
	s_add_u32 s82, s82, 0x1400000
	s_addc_u32 s83, s83, 0
	s_lshl_b32 s85, s81, 7
	s_add_u32 s98, s50, s85
	s_addc_u32 s99, s51, 0
	s_add_u32 s98, s98, 0xfc00000
	s_addc_u32 s99, s99, 0
	v_mov_b32_e32 v250, 0x358637bd
	s_waitcnt vmcnt(0)
	global_store_dwordx4 v236, v[216:219], s[98:99]
	global_store_dwordx4 v236, v[220:223], s[98:99] offset:1024
	v_lshlrev_b32_e32 v240, 16, v200
	v_and_b32_e32 v241, 0xffff0000, v200
	v_lshlrev_b32_e32 v242, 16, v201
	v_and_b32_e32 v243, 0xffff0000, v201
	v_lshlrev_b32_e32 v244, 16, v202
	v_and_b32_e32 v245, 0xffff0000, v202
	v_lshlrev_b32_e32 v246, 16, v203
	v_and_b32_e32 v247, 0xffff0000, v203
	v_pk_mul_f32 v[248:249], v[240:241], v[240:241]
	v_pk_fma_f32 v[248:249], v[242:243], v[242:243], v[248:249]
	v_pk_fma_f32 v[248:249], v[244:245], v[244:245], v[248:249]
	v_pk_fma_f32 v[248:249], v[246:247], v[246:247], v[248:249]
	s_nop 0
	v_add_f32_e32 v248, v248, v249
	s_nop 1
	v_add_f32_dpp v248, v248, v248 quad_perm:[1,0,3,2] row_mask:0xf bank_mask:0xf
	s_nop 1
	v_add_f32_dpp v248, v248, v248 quad_perm:[2,3,0,1] row_mask:0xf bank_mask:0xf
	s_nop 1
	v_add_f32_dpp v248, v248, v248 row_ror:4 row_mask:0xf bank_mask:0xf
	s_nop 1
	v_add_f32_dpp v248, v248, v248 row_ror:8 row_mask:0xf bank_mask:0xf
	s_nop 0
	v_fmamk_f32 v248, v248, 0x3c000000, v250
	v_rsq_f32_e32 v248, v248
	s_nop 0
	v_pk_mul_f32 v[240:241], v[248:249], v[240:241] op_sel_hi:[0,1]
	v_pk_mul_f32 v[242:243], v[248:249], v[242:243] op_sel_hi:[0,1]
	v_pk_mul_f32 v[244:245], v[248:249], v[244:245] op_sel_hi:[0,1]
	v_pk_mul_f32 v[246:247], v[248:249], v[246:247] op_sel_hi:[0,1]
	v_pk_mul_f32 v[240:241], v[224:225], v[240:241]
	v_pk_mul_f32 v[242:243], v[226:227], v[242:243]
	v_pk_mul_f32 v[244:245], v[228:229], v[244:245]
	v_pk_mul_f32 v[246:247], v[230:231], v[246:247]
	v_cvt_pk_bf16_f32 v200, v240, v241
	v_cvt_pk_bf16_f32 v201, v242, v243
	v_cvt_pk_bf16_f32 v202, v244, v245
	v_cvt_pk_bf16_f32 v203, v246, v247
	global_store_dwordx4 v235, v[200:203], s[82:83]
	v_lshlrev_b32_e32 v240, 16, v204
	v_and_b32_e32 v241, 0xffff0000, v204
	v_lshlrev_b32_e32 v242, 16, v205
	v_and_b32_e32 v243, 0xffff0000, v205
	v_lshlrev_b32_e32 v244, 16, v206
	v_and_b32_e32 v245, 0xffff0000, v206
	v_lshlrev_b32_e32 v246, 16, v207
	v_and_b32_e32 v247, 0xffff0000, v207
	v_pk_mul_f32 v[248:249], v[240:241], v[240:241]
	v_pk_fma_f32 v[248:249], v[242:243], v[242:243], v[248:249]
	v_pk_fma_f32 v[248:249], v[244:245], v[244:245], v[248:249]
	v_pk_fma_f32 v[248:249], v[246:247], v[246:247], v[248:249]
	s_nop 0
	v_add_f32_e32 v248, v248, v249
	s_nop 1
	v_add_f32_dpp v248, v248, v248 quad_perm:[1,0,3,2] row_mask:0xf bank_mask:0xf
	s_nop 1
	v_add_f32_dpp v248, v248, v248 quad_perm:[2,3,0,1] row_mask:0xf bank_mask:0xf
	s_nop 1
	v_add_f32_dpp v248, v248, v248 row_ror:4 row_mask:0xf bank_mask:0xf
	s_nop 1
	v_add_f32_dpp v248, v248, v248 row_ror:8 row_mask:0xf bank_mask:0xf
	s_nop 0
	v_fmamk_f32 v248, v248, 0x3c000000, v250
	v_rsq_f32_e32 v248, v248
	s_nop 0
	v_pk_mul_f32 v[240:241], v[248:249], v[240:241] op_sel_hi:[0,1]
	v_pk_mul_f32 v[242:243], v[248:249], v[242:243] op_sel_hi:[0,1]
	v_pk_mul_f32 v[244:245], v[248:249], v[244:245] op_sel_hi:[0,1]
	v_pk_mul_f32 v[246:247], v[248:249], v[246:247] op_sel_hi:[0,1]
	v_pk_mul_f32 v[240:241], v[224:225], v[240:241]
	v_pk_mul_f32 v[242:243], v[226:227], v[242:243]
	v_pk_mul_f32 v[244:245], v[228:229], v[244:245]
	v_pk_mul_f32 v[246:247], v[230:231], v[246:247]
	v_cvt_pk_bf16_f32 v204, v240, v241
	v_cvt_pk_bf16_f32 v205, v242, v243
	v_cvt_pk_bf16_f32 v206, v244, v245
	v_cvt_pk_bf16_f32 v207, v246, v247
	global_store_dwordx4 v235, v[204:207], s[82:83] offset:1024
	v_lshlrev_b32_e32 v240, 16, v208
	v_and_b32_e32 v241, 0xffff0000, v208
	v_lshlrev_b32_e32 v242, 16, v209
	v_and_b32_e32 v243, 0xffff0000, v209
	v_lshlrev_b32_e32 v244, 16, v210
	v_and_b32_e32 v245, 0xffff0000, v210
	v_lshlrev_b32_e32 v246, 16, v211
	v_and_b32_e32 v247, 0xffff0000, v211
	v_pk_mul_f32 v[248:249], v[240:241], v[240:241]
	v_pk_fma_f32 v[248:249], v[242:243], v[242:243], v[248:249]
	v_pk_fma_f32 v[248:249], v[244:245], v[244:245], v[248:249]
	v_pk_fma_f32 v[248:249], v[246:247], v[246:247], v[248:249]
	s_nop 0
	v_add_f32_e32 v248, v248, v249
	s_nop 1
	v_add_f32_dpp v248, v248, v248 quad_perm:[1,0,3,2] row_mask:0xf bank_mask:0xf
	s_nop 1
	v_add_f32_dpp v248, v248, v248 quad_perm:[2,3,0,1] row_mask:0xf bank_mask:0xf
	s_nop 1
	v_add_f32_dpp v248, v248, v248 row_ror:4 row_mask:0xf bank_mask:0xf
	s_nop 1
	v_add_f32_dpp v248, v248, v248 row_ror:8 row_mask:0xf bank_mask:0xf
	s_nop 0
	v_fmamk_f32 v248, v248, 0x3c000000, v250
	v_rsq_f32_e32 v248, v248
	s_nop 0
	v_pk_mul_f32 v[240:241], v[248:249], v[240:241] op_sel_hi:[0,1]
	v_pk_mul_f32 v[242:243], v[248:249], v[242:243] op_sel_hi:[0,1]
	v_pk_mul_f32 v[244:245], v[248:249], v[244:245] op_sel_hi:[0,1]
	v_pk_mul_f32 v[246:247], v[248:249], v[246:247] op_sel_hi:[0,1]
	v_pk_mul_f32 v[240:241], v[224:225], v[240:241]
	v_pk_mul_f32 v[242:243], v[226:227], v[242:243]
	v_pk_mul_f32 v[244:245], v[228:229], v[244:245]
	v_pk_mul_f32 v[246:247], v[230:231], v[246:247]
	v_cvt_pk_bf16_f32 v208, v240, v241
	v_cvt_pk_bf16_f32 v209, v242, v243
	v_cvt_pk_bf16_f32 v210, v244, v245
	v_cvt_pk_bf16_f32 v211, v246, v247
	global_store_dwordx4 v235, v[208:211], s[82:83] offset:2048
	v_lshlrev_b32_e32 v240, 16, v212
	v_and_b32_e32 v241, 0xffff0000, v212
	v_lshlrev_b32_e32 v242, 16, v213
	v_and_b32_e32 v243, 0xffff0000, v213
	v_lshlrev_b32_e32 v244, 16, v214
	v_and_b32_e32 v245, 0xffff0000, v214
	v_lshlrev_b32_e32 v246, 16, v215
	v_and_b32_e32 v247, 0xffff0000, v215
	v_pk_mul_f32 v[248:249], v[240:241], v[240:241]
	v_pk_fma_f32 v[248:249], v[242:243], v[242:243], v[248:249]
	v_pk_fma_f32 v[248:249], v[244:245], v[244:245], v[248:249]
	v_pk_fma_f32 v[248:249], v[246:247], v[246:247], v[248:249]
	s_nop 0
	v_add_f32_e32 v248, v248, v249
	s_nop 1
	v_add_f32_dpp v248, v248, v248 quad_perm:[1,0,3,2] row_mask:0xf bank_mask:0xf
	s_nop 1
	v_add_f32_dpp v248, v248, v248 quad_perm:[2,3,0,1] row_mask:0xf bank_mask:0xf
	s_nop 1
	v_add_f32_dpp v248, v248, v248 row_ror:4 row_mask:0xf bank_mask:0xf
	s_nop 1
	v_add_f32_dpp v248, v248, v248 row_ror:8 row_mask:0xf bank_mask:0xf
	s_nop 0
	v_fmamk_f32 v248, v248, 0x3c000000, v250
	v_rsq_f32_e32 v248, v248
	s_nop 0
	v_pk_mul_f32 v[240:241], v[248:249], v[240:241] op_sel_hi:[0,1]
	v_pk_mul_f32 v[242:243], v[248:249], v[242:243] op_sel_hi:[0,1]
	v_pk_mul_f32 v[244:245], v[248:249], v[244:245] op_sel_hi:[0,1]
	v_pk_mul_f32 v[246:247], v[248:249], v[246:247] op_sel_hi:[0,1]
	v_pk_mul_f32 v[240:241], v[224:225], v[240:241]
	v_pk_mul_f32 v[242:243], v[226:227], v[242:243]
	v_pk_mul_f32 v[244:245], v[228:229], v[244:245]
	v_pk_mul_f32 v[246:247], v[230:231], v[246:247]
	v_cvt_pk_bf16_f32 v212, v240, v241
	v_cvt_pk_bf16_f32 v213, v242, v243
	v_cvt_pk_bf16_f32 v214, v244, v245
	v_cvt_pk_bf16_f32 v215, v246, v247
	global_store_dwordx4 v235, v[212:215], s[82:83] offset:3072

.LBB0_473:
.LBB0_479:
	s_cmp_gt_i32 s89, 3
	s_cbranch_scc0 .LBB0_533
	s_waitcnt vmcnt(0)
	s_waitcnt vmcnt(0)
	s_barrier
	s_and_saveexec_b64 s[0:1], s[94:95]
	s_cbranch_execz .LBB0_532
	s_add_i32 s4, 0, 0x26d60
	v_mov_b32_e32 v1, s4
	s_waitcnt vmcnt(0) expcnt(0) lgkmcnt(0)
	ds_read_b32 v3, v1
	s_add_i32 s4, 0, 0x26d64
	v_mov_b32_e32 v1, s4
	ds_read_b32 v1, v1
	s_waitcnt lgkmcnt(1)
	v_cmp_ne_u32_e32 vcc, 0, v3
	s_cbranch_vccnz .LBB0_496
	v_readlane_b32 s4, v252, 0
	v_readlane_b32 s5, v252, 1
	s_load_dwordx2 s[12:13], s[4:5], 0x4
	s_add_u32 s4, s86, 0x1000
	s_addc_u32 s5, s87, 0
	s_add_u32 s10, s86, 0x1100
	s_addc_u32 s11, s87, 0
	s_waitcnt lgkmcnt(0)
	s_mul_i32 s22, s12, s84
	s_add_u32 s12, s86, 0x1200
	s_mul_i32 s22, s22, s13
	s_addc_u32 s13, s87, 0
	s_add_u32 s14, s86, 0x1300
	s_addc_u32 s15, s87, 0
	s_mov_b32 s23, 1
	v_mov_b32_e32 v17, 0
	s_branch .LBB0_484
